# in-proj: the next tile's first k-tile is requested by LDS-DMA before the current tile's epilogue (the epilogue does not use the LDS)
# speedup vs baseline: 1.0339x; 1.0020x over previous
; #define CAS __attribute__((address_space(4)))
;     template <class T> __device__ __forceinline__ T* w(size_t off) const { return (T*)(p->ws + off); }
; __global__ void __launch_bounds__(NTHR, 2) mk_fwd(Params prm) {
;     __shared__ __attribute__((aligned(16))) unsigned char smem_raw[S3_LDS_END];
;     float* smem = (float*)(smem_raw + GEMM_LDS);
;     Ctx c; c.p = (const CAS Params*)__builtin_amdgcn_kernarg_segment_ptr(); c.smf = smem; c.tid = threadIdx.x;
;     const int G = gridDim.x, bid = blockIdx.x;
;     const int gthreads = G * NTHR, nwaves = gthreads >> 6;
;     ...
;     int* smi = (int*)(smem + 16);
;     ...
;     volatile unsigned* bst = (volatile unsigned*)(smem + 120);
;     if (c.tid == 0) { bst[0] = 0u; bst[1] = 0u; }
;     __syncthreads();
;     XcdBarrier bar = xcd_barrier_post(c.w<unsigned>(WS_CTL) + CW_BAR, bst);
.LBB0_13:
	s_mov_b32 s101, 0
	ds_read_b32 v2, v146
	s_waitcnt lgkmcnt(0)
	v_readfirstlane_b32 s7, v2
	s_cmp_eq_u32 s7, 0
	s_cbranch_scc1 .Lstag_done
	s_lshr_b32 s6, 0x10884, s66
	s_bitcmp1_b32 s6, 0
	s_cbranch_scc0 .Lstag_n0
	s_sleep 14

;     const int lane = tid & 63, wid = tid >> 6, wr = wid >> 1, wc = wid & 1, fr = lane & 15, fq = lane >> 4;
; #pragma unroll
;     for (int m = 0; m < 4; ++m)
; #pragma unroll
;         for (int n = 0; n < 4; ++n) acc[m][n] = (f32x4){0.f, 0.f, 0.f, 0.f};
;     unsigned ao[4];
; #pragma unroll
;     for (int i = 0; i < 4; ++i) ao[i] = arow((tid >> 3) + 32 * i) + (tid & 7) * 8;
;     const int bk = tid >> 4, bnc = tid & 15;
;     constexpr int NRB = B_F32 ? 8 : 4;
;     u32x4 ra0[4], ra1[4]; u32x4 rb0[NRB], rb1[NRB];
;     auto gloadA = [&](int kt, u32x4 (&ra)[4]) __attribute__((always_inline)) {
; #pragma unroll
;         for (int i = 0; i < 4; ++i) ra[i] = *(const u32x4*)(Abase + (ao[i] + kt * 64));
;     };
;     auto gloadB = [&](int kt, u32x4 (&rb)[NRB]) __attribute__((always_inline)) {
;         if (B_F32) {
;             const float* bp = (const float*)Bbase + (boff + (unsigned)((kt * 64 + bk) * ldb));
; #pragma unroll
;             for (int i = 0; i < 4; ++i) {
;                 if (bval) { rb[2 * i] = *(const u32x4*)(bp + (unsigned)(16 * i * ldb)); rb[2 * i + 1] = *(const u32x4*)(bp + (unsigned)(16 * i * ldb) + 4); }
;                 else { rb[2 * i] = (u32x4){0u, 0u, 0u, 0u}; rb[2 * i + 1] = rb[2 * i]; }
;             }
;         } else {
;             const bf16* bp = (const bf16*)Bbase + (boff + (unsigned)((kt * 64 + bk) * ldb));
; #pragma unroll
;             for (int i = 0; i < 4; ++i) rb[i] = bval ? *(const u32x4*)(bp + (unsigned)(16 * i * ldb)) : (u32x4){0u, 0u, 0u, 0u};
;         }
;     };
;     auto lstore = [&](const u32x4 (&ra)[4], const u32x4 (&rb)[NRB]) __attribute__((always_inline)) {
; #pragma unroll
;         for (int i = 0; i < 4; ++i) { const int row = (tid >> 3) + 32 * i, kc = tid & 7;
;             const u32x4 v = (kc & 1) ? (u32x4){ra[i][2], ra[i][3], ra[i][0], ra[i][1]} : ra[i];
; __device__ __forceinline__ void ph_inproj_mfma(const Ctx& c, int layer, int tile, unsigned char* lds) {
;     const int mt = tile / 18, nt = tile % 18;
;     const bf16* HA = c.w<bf16>(WS_HA) + (size_t)mt * 128 * D;
;     f32x4 acc[4][4];
;     const int vc = nt * 128 + (c.tid & 15) * 8;
;     gemm_tile<false, 1>(c.tid, lds, HA, [&](int r) __attribute__((always_inline)) { return (unsigned)(r * D); }, c.w<bf16>(WS_BIN) + (size_t)layer * D * DINV, (unsigned)vc, DINV, true, D, acc);
.LBB0_544:
	s_andn2_b64 vcc, exec, s[0:1]
	s_cbranch_vccnz .LBB0_533
	s_mul_hi_i32 s0, s60, 0x38e38e39
	s_load_dwordx2 s[42:43], s[4:5], 0x130
	s_lshr_b32 s1, s0, 31
	s_ashr_i32 s0, s0, 2
	s_add_i32 s28, s0, s1
	s_mul_i32 s0, s28, 18
	s_ashr_i32 s29, s28, 31
	s_sub_i32 s17, s60, s0
	s_lshl_b64 s[0:1], s[28:29], 18
	s_waitcnt lgkmcnt(0)
	s_add_u32 s0, s42, s0
	s_addc_u32 s1, s43, s1
	s_add_u32 s44, s0, 0x45c6000
	s_addc_u32 s45, s1, 0
	s_lshl_b32 s61, s17, 7
	s_add_u32 s0, s42, s59
	s_waitcnt vmcnt(0)
	v_lshlrev_b32_e32 v12, 3, v147
	s_addc_u32 s1, s43, s58
	s_add_u32 s46, s0, 0x18095100
	v_lshlrev_b32_e32 v2, 7, v147
	v_and_b32_e32 v4, 56, v12
	s_movk_i32 s0, 0xfc00
	v_and_b32_e32 v155, 15, v147
	v_and_or_b32 v2, v2, s0, v4
	v_lshrrev_b32_e32 v5, 1, v147
	s_mov_b32 s0, 0x3ffffc0
	v_bfe_u32 v157, v147, 4, 2
	v_and_or_b32 v5, v5, s0, v155
	v_bfe_u32 v7, v147, 4, 1
	v_lshlrev_b32_e32 v16, 6, v5
	v_lshlrev_b32_e32 v118, 3, v157
	v_bfe_u32 v5, v147, 2, 2
	v_lshlrev_b32_e32 v9, 2, v7
	v_or3_b32 v5, v9, v5, v118
	v_lshlrev_b32_e32 v9, 1, v147
	v_and_b32_e32 v9, 0x80, v9
	s_movk_i32 s7, 0x120
	v_mad_u32_u24 v5, v5, s7, v9
	v_and_b32_e32 v13, 0x78, v12
	v_add_u32_e32 v4, 0x8000, v2
	v_add_u32_e32 v6, 0x10000, v2
	v_ashrrev_i32_e32 v15, 4, v147
	v_and_or_b32 v119, v12, 24, v5
	v_cmp_eq_u32_e32 vcc, 0, v7
	v_mov_b32_e32 v5, v3
	v_mov_b32_e32 v7, v3
	s_movk_i32 s0, 0x900
	v_or_b32_e32 v14, s61, v13
	v_lshl_add_u64 v[4:5], v[4:5], 1, s[44:45]
	v_lshl_add_u64 v[6:7], v[6:7], 1, s[44:45]
	v_mul_lo_u32 v18, v15, s0
	s_addc_u32 s47, s1, 0
	v_add_u32_e32 v8, 0x18000, v2
	v_mov_b32_e32 v9, v3
	v_add_u32_e32 v6, v14, v18
	v_mov_b32_e32 v7, v3
	v_lshl_add_u64 v[4:5], v[8:9], 1, s[44:45]
	v_lshl_add_u64 v[6:7], v[6:7], 1, s[46:47]
	s_mov_b32 s0, 0x12000
	v_cndmask_b32_e32 v17, v236, v237, vcc
	v_add_co_u32_e32 v4, vcc, s0, v6
	s_mov_b32 s0, 0x24000
	s_nop 0
	v_addc_co_u32_e32 v5, vcc, 0, v7, vcc
	v_add_co_u32_e32 v8, vcc, s0, v6
	s_mov_b32 s0, 0x36000
	s_nop 0
	v_addc_co_u32_e32 v9, vcc, 0, v7, vcc
	v_add_co_u32_e32 v4, vcc, s0, v6
	v_lshl_add_u64 v[10:11], v[2:3], 1, s[44:45]
	s_nop 0
	v_addc_co_u32_e32 v5, vcc, 0, v7, vcc
	v_add_u32_e32 v6, 0x8040, v2
	v_mov_b32_e32 v7, v3
	v_lshl_add_u64 v[6:7], v[6:7], 1, s[44:45]
	v_add_u32_e32 v4, 0x10040, v2
	v_mov_b32_e32 v5, v3
	v_lshl_add_u64 v[4:5], v[4:5], 1, s[44:45]
	v_add_u32_e32 v6, 0x18040, v2
	v_mov_b32_e32 v7, v3
	v_lshl_add_u64 v[6:7], v[6:7], 1, s[44:45]
	v_and_b32_e32 v4, 1, v147
	v_cmp_eq_u32_e64 s[0:1], 0, v4
	v_bfe_i32 v4, v147, 2, 1
	v_and_b32_e32 v4, 0x2040, v4
	v_and_b32_e32 v5, 0xffffffc0, v12
	v_lshl_add_u32 v7, s60, 7, v18
	v_add_u32_e32 v4, v4, v5
	v_lshlrev_b32_e32 v5, 4, v147
	v_mul_lo_u32 v6, v15, s7
	v_or_b32_e32 v7, v7, v13
	s_mul_i32 s7, s28, 0x900
	v_lshlrev_b32_e32 v122, 4, v157
	v_and_b32_e32 v5, 48, v5
	v_lshlrev_b32_e32 v153, 4, v155
	v_subrev_u32_e32 v7, s7, v7
	v_mov_b32_e32 v20, 0
	v_lshrrev_b32_e32 v149, 4, v147
	s_mov_b32 s6, 0
	v_add_u32_e32 v116, 0x48000, v7
	v_add_u32_e32 v120, 0x10080, v2
	v_add_u32_e32 v123, v4, v5
	v_add_u32_e32 v124, v6, v153
	v_add_u32_e32 v125, v16, v122
	v_add_u32_e32 v126, v119, v17
	v_bfe_u32 v120, v147, 2, 2
	v_sub_u32_e32 v120, 0, v120
	v_and_b32_e32 v120, 3, v120
	v_lshlrev_b32_e32 v120, 4, v120
	v_xor_b32_e32 v216, v125, v120
	v_bfe_u32 v120, v147, 4, 2
	v_lshlrev_b32_e32 v120, 3, v120
	v_bfe_u32 v121, v147, 2, 2
	v_add_u32_e32 v120, v120, v121
	v_lshlrev_b32_e32 v120, 8, v120
	v_lshrrev_b32_e32 v68, 6, v147
	v_lshrrev_b32_e32 v214, 4, v147
	v_xor_b32_e32 v68, v68, v214
	v_and_b32_e32 v68, 1, v68
	v_lshlrev_b32_e32 v68, 7, v68
	v_or_b32_e32 v120, v120, v68
	v_and_b32_e32 v68, 3, v147
	v_lshlrev_b32_e32 v68, 3, v68
	v_or_b32_e32 v120, v120, v68
	v_xor_b32_e32 v68, 0, v121
	v_lshl_or_b32 v214, v68, 5, v120
	v_xor_b32_e32 v68, 1, v121
	v_lshl_or_b32 v215, v68, 5, v120
	v_xor_b32_e32 v68, 2, v121
	v_lshl_or_b32 v217, v68, 5, v120
	v_xor_b32_e32 v68, 3, v121
	v_lshl_or_b32 v218, v68, 5, v120
	v_lshrrev_b32_e32 v120, 6, v147
	s_nop 1
	v_readfirstlane_b32 s98, v120
	s_nop 1
	s_lshl_b32 s99, s98, 12
	s_lshl_b32 s98, s98, 11
	s_lshl_b32 s100, s61, 1
	s_add_u32 s46, s46, s100
	s_addc_u32 s47, s47, 0
	v_lshrrev_b32_e32 v120, 6, v147
	v_lshlrev_b32_e32 v120, 5, v120
	v_bfe_u32 v121, v147, 2, 4
	v_add_u32_e32 v120, v120, v121
	v_mul_u32_u24_e32 v120, 0x800, v120
	v_bfe_u32 v121, v147, 4, 2
	v_sub_u32_e32 v121, 0, v121
	v_and_b32_e32 v121, 3, v121
	v_and_b32_e32 v68, 3, v147
	v_xor_b32_e32 v121, v121, v68
	v_lshl_add_u32 v206, v121, 4, v120
	v_add_u32_e32 v207, 64, v206
	v_add_u32_e32 v208, 0x8000, v206
	v_add_u32_e32 v209, 64, v208
	v_lshrrev_b32_e32 v120, 6, v147
	v_lshlrev_b32_e32 v120, 4, v120
	v_bfe_u32 v121, v147, 4, 2
	v_add_u32_e32 v120, v120, v121
	v_mul_u32_u24_e32 v120, 0x1200, v120
	v_bfe_u32 v68, v147, 1, 3
	v_xor_b32_e32 v68, v68, v121
	v_lshlrev_b32_e32 v68, 1, v68
	v_and_b32_e32 v121, 1, v147
	v_or_b32_e32 v68, v68, v121
	v_lshl_add_u32 v210, v68, 4, v120
	v_add_u32_e32 v211, 0x4800, v210
	v_xor_b32_e32 v68, 8, v68
	v_lshl_add_u32 v212, v68, 4, v120
	v_add_u32_e32 v212, 0x9000, v212
	v_add_u32_e32 v213, 0x4800, v212
	s_cmp_lg_u32 s101, 0
	s_cbranch_scc1 .Lip_havepf
	s_barrier
	s_add_u32 m0, s98, 0x0
	s_nop 0
	global_load_lds_dwordx4 v206, s[44:45]
	s_add_u32 m0, s98, 0x2040
	s_nop 0
	global_load_lds_dwordx4 v207, s[44:45]
	s_add_u32 m0, s98, 0x400
	s_nop 0
	global_load_lds_dwordx4 v208, s[44:45]
	s_add_u32 m0, s98, 0x2440
	s_nop 0
	global_load_lds_dwordx4 v209, s[44:45]
	s_add_u32 m0, s99, 0x4080
	s_nop 0
	global_load_lds_dwordx4 v210, s[46:47]
	s_add_u32 m0, s99, 0x4480
	s_nop 0
	global_load_lds_dwordx4 v211, s[46:47]
	s_add_u32 m0, s99, 0x4880
	s_nop 0
	global_load_lds_dwordx4 v212, s[46:47]
	s_add_u32 m0, s99, 0x4c80
	s_nop 0
	global_load_lds_dwordx4 v213, s[46:47]
; #define LAS __attribute__((address_space(3)))
; __device__ __forceinline__ s16x4 lds_tr(lds_cptr p) { return __builtin_bit_cast(s16x4, __builtin_amdgcn_ds_read_tr16_b64_v4i16((LAS s16x4*)p)); }
;     ...
;     auto compute = [&]() __attribute__((always_inline)) {
; #pragma unroll
;         for (int kh = 0; kh < 2; ++kh) {
;             bf16x8 af[4], bfr[4];
; #pragma unroll
;             for (int m = 0; m < 4; ++m) af[m] = *(const LAS bf16x8*)(la + kh * GA_KH + m * 1024);
; #pragma unroll
;             for (int n = 0; n < 4; ++n) {
;                 const s16x4 r0 = lds_tr(lb + kh * 32 * GB_ST + n * 32), r1 = lds_tr(lb + kh * 32 * GB_ST + n * 32 + bsw);
;                 bfr[n] = (bf16x8){r0[0], r0[1], r0[2], r0[3], r1[0], r1[1], r1[2], r1[3]};
;             }
; #pragma unroll
;             for (int m = 0; m < 4; ++m)
; #pragma unroll
;                 for (int n = 0; n < 4; ++n) acc[m][n] = __builtin_amdgcn_mfma_f32_16x16x32_bf16(bfr[n], af[m], acc[m][n], 0, 0, 0);
;         }
;     };
;     ...
;     if (DEEP == 1) {
;         gloadA(0, ra0); gloadB(0, rb0); gloadA(1, ra1);
;         for (int kt = 0; kt < nk; kt += 2) {
;             __syncthreads();
;             lstore(ra0, rb0);
;             __syncthreads();
;             gloadB(kt + 1, rb0);
;             if (kt + 2 < nk) gloadA(kt + 2, ra0);
;             compute();
.Lip_havepf:
	s_mov_b32 s101, 0
	s_add_u32 s44, s44, 0x80
	s_addc_u32 s45, s45, 0
	s_add_u32 s46, s46, 0x48000
	s_addc_u32 s47, s47, 0
	v_mov_b32_e32 v21, v20
	v_mov_b32_e32 v22, v20
	v_mov_b32_e32 v23, v20
	v_mov_b32_e32 v32, v20
	v_mov_b32_e32 v33, v20
	v_mov_b32_e32 v34, v20
	v_mov_b32_e32 v35, v20
	v_mov_b32_e32 v4, v20
	v_mov_b32_e32 v5, v20
	v_mov_b32_e32 v6, v20
	v_mov_b32_e32 v7, v20
	v_mov_b32_e32 v8, v20
	v_mov_b32_e32 v9, v20
	v_mov_b32_e32 v10, v20
	v_mov_b32_e32 v11, v20
	v_mov_b32_e32 v12, v20
	v_mov_b32_e32 v13, v20
	v_mov_b32_e32 v14, v20
	v_mov_b32_e32 v15, v20
	v_mov_b32_e32 v16, v20
	v_mov_b32_e32 v17, v20
	v_mov_b32_e32 v18, v20
	v_mov_b32_e32 v19, v20
	v_mov_b32_e32 v24, v20
	v_mov_b32_e32 v25, v20
	v_mov_b32_e32 v26, v20
	v_mov_b32_e32 v27, v20
	v_mov_b32_e32 v28, v20
	v_mov_b32_e32 v29, v20
	v_mov_b32_e32 v30, v20
	v_mov_b32_e32 v31, v20
	v_mov_b32_e32 v36, v20
	v_mov_b32_e32 v37, v20
	v_mov_b32_e32 v38, v20
	v_mov_b32_e32 v39, v20
	v_mov_b32_e32 v40, v20
	v_mov_b32_e32 v41, v20
	v_mov_b32_e32 v42, v20
	v_mov_b32_e32 v43, v20
	v_mov_b32_e32 v44, v20
	v_mov_b32_e32 v45, v20
	v_mov_b32_e32 v46, v20
	v_mov_b32_e32 v47, v20
	v_mov_b32_e32 v48, v20
	v_mov_b32_e32 v49, v20
	v_mov_b32_e32 v50, v20
	v_mov_b32_e32 v51, v20
	v_mov_b32_e32 v52, v20
	v_mov_b32_e32 v53, v20
	v_mov_b32_e32 v54, v20
	v_mov_b32_e32 v55, v20
	v_mov_b32_e32 v56, v20
	v_mov_b32_e32 v57, v20
	v_mov_b32_e32 v58, v20
	v_mov_b32_e32 v59, v20
	v_mov_b32_e32 v60, v20
	v_mov_b32_e32 v61, v20
	v_mov_b32_e32 v62, v20
	v_mov_b32_e32 v63, v20
	v_mov_b32_e32 v64, v20
	v_mov_b32_e32 v65, v20
	v_mov_b32_e32 v66, v20
	v_mov_b32_e32 v67, v20
	s_waitcnt vmcnt(0)
	s_barrier
.Lip_loop:
	s_add_u32 m0, s98, 0x9000
	ds_read_b64_tr_b16 v[158:159], v214 offset:16512
	ds_read_b64_tr_b16 v[160:161], v214 offset:17536
	ds_read_b128 v[128:131], v216
	ds_read_b64_tr_b16 v[162:163], v215 offset:16512
	ds_read_b64_tr_b16 v[164:165], v215 offset:17536
	s_waitcnt lgkmcnt(2)
	v_mfma_f32_16x16x32_bf16 v[64:67], v[158:161], v[128:131], v[64:67]
	global_load_lds_dwordx4 v206, s[44:45]
	s_add_u32 m0, s98, 0xb040
	ds_read_b64_tr_b16 v[166:167], v217 offset:16512
	ds_read_b64_tr_b16 v[168:169], v217 offset:17536
	s_waitcnt lgkmcnt(2)
	v_mfma_f32_16x16x32_bf16 v[60:63], v[162:165], v[128:131], v[60:63]
	global_load_lds_dwordx4 v207, s[44:45]
	s_add_u32 m0, s98, 0x9400
	ds_read_b64_tr_b16 v[170:171], v218 offset:16512
	ds_read_b64_tr_b16 v[172:173], v218 offset:17536
	s_waitcnt lgkmcnt(2)
	v_mfma_f32_16x16x32_bf16 v[56:59], v[166:169], v[128:131], v[56:59]
	global_load_lds_dwordx4 v208, s[44:45]
	s_add_u32 m0, s98, 0xb440
	ds_read_b128 v[132:135], v216 offset:1024
	s_waitcnt lgkmcnt(1)
	v_mfma_f32_16x16x32_bf16 v[52:55], v[170:173], v[128:131], v[52:55]
	global_load_lds_dwordx4 v209, s[44:45]
	s_add_u32 m0, s99, 0xd080
	ds_read_b128 v[136:139], v216 offset:2048
	s_waitcnt lgkmcnt(1)
	v_mfma_f32_16x16x32_bf16 v[48:51], v[158:161], v[132:135], v[48:51]
	global_load_lds_dwordx4 v210, s[46:47]
	s_add_u32 m0, s99, 0xd480
	ds_read_b128 v[140:143], v216 offset:3072
	v_mfma_f32_16x16x32_bf16 v[44:47], v[162:165], v[132:135], v[44:47]
	global_load_lds_dwordx4 v211, s[46:47]
	s_add_u32 m0, s99, 0xd880
	ds_read_b64_tr_b16 v[174:175], v214 offset:24704
	ds_read_b64_tr_b16 v[176:177], v214 offset:25728
	v_mfma_f32_16x16x32_bf16 v[40:43], v[166:169], v[132:135], v[40:43]
	global_load_lds_dwordx4 v212, s[46:47]
	s_add_u32 m0, s99, 0xdc80
	ds_read_b64_tr_b16 v[178:179], v215 offset:24704
	ds_read_b64_tr_b16 v[180:181], v215 offset:25728
	v_mfma_f32_16x16x32_bf16 v[36:39], v[170:173], v[132:135], v[36:39]
	global_load_lds_dwordx4 v213, s[46:47]
	s_add_u32 s44, s44, 0x80
	s_addc_u32 s45, s45, 0
	s_add_u32 s46, s46, 0x48000
	s_addc_u32 s47, s47, 0
	ds_read_b128 v[128:131], v216 offset:8256
	s_waitcnt lgkmcnt(6)
	v_mfma_f32_16x16x32_bf16 v[28:31], v[158:161], v[136:139], v[28:31]
	ds_read_b64_tr_b16 v[182:183], v217 offset:24704
	ds_read_b64_tr_b16 v[184:185], v217 offset:25728
	v_mfma_f32_16x16x32_bf16 v[24:27], v[162:165], v[136:139], v[24:27]
	ds_read_b64_tr_b16 v[186:187], v218 offset:24704
	ds_read_b64_tr_b16 v[188:189], v218 offset:25728
	v_mfma_f32_16x16x32_bf16 v[16:19], v[166:169], v[136:139], v[16:19]
	v_mfma_f32_16x16x32_bf16 v[12:15], v[170:173], v[136:139], v[12:15]
	ds_read_b128 v[132:135], v216 offset:9280
	s_waitcnt lgkmcnt(10)
	v_mfma_f32_16x16x32_bf16 v[8:11], v[158:161], v[140:143], v[8:11]
	v_mfma_f32_16x16x32_bf16 v[4:7], v[162:165], v[140:143], v[4:7]
	v_mfma_f32_16x16x32_bf16 v[32:35], v[166:169], v[140:143], v[32:35]
	v_mfma_f32_16x16x32_bf16 v[20:23], v[170:173], v[140:143], v[20:23]
	ds_read_b128 v[136:139], v216 offset:10304
	s_waitcnt lgkmcnt(6)
	v_mfma_f32_16x16x32_bf16 v[64:67], v[174:177], v[128:131], v[64:67]
	v_mfma_f32_16x16x32_bf16 v[60:63], v[178:181], v[128:131], v[60:63]
	s_waitcnt lgkmcnt(4)
	v_mfma_f32_16x16x32_bf16 v[56:59], v[182:185], v[128:131], v[56:59]
	s_waitcnt lgkmcnt(2)
	v_mfma_f32_16x16x32_bf16 v[52:55], v[186:189], v[128:131], v[52:55]
	ds_read_b128 v[140:143], v216 offset:11328
	s_waitcnt lgkmcnt(2)
	v_mfma_f32_16x16x32_bf16 v[48:51], v[174:177], v[132:135], v[48:51]
	v_mfma_f32_16x16x32_bf16 v[44:47], v[178:181], v[132:135], v[44:47]
	v_mfma_f32_16x16x32_bf16 v[40:43], v[182:185], v[132:135], v[40:43]
	v_mfma_f32_16x16x32_bf16 v[36:39], v[186:189], v[132:135], v[36:39]
	s_waitcnt lgkmcnt(1)
	v_mfma_f32_16x16x32_bf16 v[28:31], v[174:177], v[136:139], v[28:31]
	v_mfma_f32_16x16x32_bf16 v[24:27], v[178:181], v[136:139], v[24:27]
	v_mfma_f32_16x16x32_bf16 v[16:19], v[182:185], v[136:139], v[16:19]
	v_mfma_f32_16x16x32_bf16 v[12:15], v[186:189], v[136:139], v[12:15]
	s_waitcnt lgkmcnt(0)
	v_mfma_f32_16x16x32_bf16 v[8:11], v[174:177], v[140:143], v[8:11]
	v_mfma_f32_16x16x32_bf16 v[4:7], v[178:181], v[140:143], v[4:7]
	v_mfma_f32_16x16x32_bf16 v[32:35], v[182:185], v[140:143], v[32:35]
	v_mfma_f32_16x16x32_bf16 v[20:23], v[186:189], v[140:143], v[20:23]
	s_waitcnt vmcnt(0) lgkmcnt(0)
	s_barrier
; #define LAS __attribute__((address_space(3)))
; __device__ __forceinline__ s16x4 lds_tr(lds_cptr p) { return __builtin_bit_cast(s16x4, __builtin_amdgcn_ds_read_tr16_b64_v4i16((LAS s16x4*)p)); }
;     ...
;     auto compute = [&]() __attribute__((always_inline)) {
; #pragma unroll
;         for (int kh = 0; kh < 2; ++kh) {
;             bf16x8 af[4], bfr[4];
; #pragma unroll
;             for (int m = 0; m < 4; ++m) af[m] = *(const LAS bf16x8*)(la + kh * GA_KH + m * 1024);
; #pragma unroll
;             for (int n = 0; n < 4; ++n) {
;                 const s16x4 r0 = lds_tr(lb + kh * 32 * GB_ST + n * 32), r1 = lds_tr(lb + kh * 32 * GB_ST + n * 32 + bsw);
;                 bfr[n] = (bf16x8){r0[0], r0[1], r0[2], r0[3], r1[0], r1[1], r1[2], r1[3]};
;             }
; #pragma unroll
;             for (int m = 0; m < 4; ++m)
; #pragma unroll
;                 for (int n = 0; n < 4; ++n) acc[m][n] = __builtin_amdgcn_mfma_f32_16x16x32_bf16(bfr[n], af[m], acc[m][n], 0, 0, 0);
;         }
;     };
;     ...
;             __syncthreads();
;             lstore(ra1, rb0);
;             __syncthreads();
;             if (kt + 2 < nk) gloadB(kt + 2, rb0);
;             if (kt + 3 < nk) gloadA(kt + 3, ra1);
;             compute();
;         }
;         return;
;     }
	s_add_u32 m0, s98, 0x0
	ds_read_b64_tr_b16 v[158:159], v214 offset:53376
	ds_read_b64_tr_b16 v[160:161], v214 offset:54400
	ds_read_b128 v[128:131], v216 offset:36864
	ds_read_b64_tr_b16 v[162:163], v215 offset:53376
	ds_read_b64_tr_b16 v[164:165], v215 offset:54400
	s_waitcnt lgkmcnt(2)
	v_mfma_f32_16x16x32_bf16 v[64:67], v[158:161], v[128:131], v[64:67]
	global_load_lds_dwordx4 v206, s[44:45]
	s_add_u32 m0, s98, 0x2040
	ds_read_b64_tr_b16 v[166:167], v217 offset:53376
	ds_read_b64_tr_b16 v[168:169], v217 offset:54400
	s_waitcnt lgkmcnt(2)
	v_mfma_f32_16x16x32_bf16 v[60:63], v[162:165], v[128:131], v[60:63]
	global_load_lds_dwordx4 v207, s[44:45]
	s_add_u32 m0, s98, 0x400
	ds_read_b64_tr_b16 v[170:171], v218 offset:53376
	ds_read_b64_tr_b16 v[172:173], v218 offset:54400
	s_waitcnt lgkmcnt(2)
	v_mfma_f32_16x16x32_bf16 v[56:59], v[166:169], v[128:131], v[56:59]
	global_load_lds_dwordx4 v208, s[44:45]
	s_add_u32 m0, s98, 0x2440
	ds_read_b128 v[132:135], v216 offset:37888
	s_waitcnt lgkmcnt(1)
	v_mfma_f32_16x16x32_bf16 v[52:55], v[170:173], v[128:131], v[52:55]
	global_load_lds_dwordx4 v209, s[44:45]
	s_add_u32 m0, s99, 0x4080
	ds_read_b128 v[136:139], v216 offset:38912
	s_waitcnt lgkmcnt(1)
	v_mfma_f32_16x16x32_bf16 v[48:51], v[158:161], v[132:135], v[48:51]
	global_load_lds_dwordx4 v210, s[46:47]
	s_add_u32 m0, s99, 0x4480
	ds_read_b128 v[140:143], v216 offset:39936
	v_mfma_f32_16x16x32_bf16 v[44:47], v[162:165], v[132:135], v[44:47]
	global_load_lds_dwordx4 v211, s[46:47]
	s_add_u32 m0, s99, 0x4880
	ds_read_b64_tr_b16 v[174:175], v214 offset:61568
	ds_read_b64_tr_b16 v[176:177], v214 offset:62592
	v_mfma_f32_16x16x32_bf16 v[40:43], v[166:169], v[132:135], v[40:43]
	global_load_lds_dwordx4 v212, s[46:47]
	s_add_u32 m0, s99, 0x4c80
	ds_read_b64_tr_b16 v[178:179], v215 offset:61568
	ds_read_b64_tr_b16 v[180:181], v215 offset:62592
	v_mfma_f32_16x16x32_bf16 v[36:39], v[170:173], v[132:135], v[36:39]
	global_load_lds_dwordx4 v213, s[46:47]
	s_add_u32 s44, s44, 0x80
	s_addc_u32 s45, s45, 0
	s_add_u32 s46, s46, 0x48000
	s_addc_u32 s47, s47, 0
	ds_read_b128 v[128:131], v216 offset:45120
	s_waitcnt lgkmcnt(6)
	v_mfma_f32_16x16x32_bf16 v[28:31], v[158:161], v[136:139], v[28:31]
	ds_read_b64_tr_b16 v[182:183], v217 offset:61568
	ds_read_b64_tr_b16 v[184:185], v217 offset:62592
	v_mfma_f32_16x16x32_bf16 v[24:27], v[162:165], v[136:139], v[24:27]
	ds_read_b64_tr_b16 v[186:187], v218 offset:61568
	ds_read_b64_tr_b16 v[188:189], v218 offset:62592
	v_mfma_f32_16x16x32_bf16 v[16:19], v[166:169], v[136:139], v[16:19]
	v_mfma_f32_16x16x32_bf16 v[12:15], v[170:173], v[136:139], v[12:15]
	ds_read_b128 v[132:135], v216 offset:46144
	s_waitcnt lgkmcnt(10)
	v_mfma_f32_16x16x32_bf16 v[8:11], v[158:161], v[140:143], v[8:11]
	v_mfma_f32_16x16x32_bf16 v[4:7], v[162:165], v[140:143], v[4:7]
	v_mfma_f32_16x16x32_bf16 v[32:35], v[166:169], v[140:143], v[32:35]
	v_mfma_f32_16x16x32_bf16 v[20:23], v[170:173], v[140:143], v[20:23]
	ds_read_b128 v[136:139], v216 offset:47168
	s_waitcnt lgkmcnt(6)
	v_mfma_f32_16x16x32_bf16 v[64:67], v[174:177], v[128:131], v[64:67]
	v_mfma_f32_16x16x32_bf16 v[60:63], v[178:181], v[128:131], v[60:63]
	s_waitcnt lgkmcnt(4)
	v_mfma_f32_16x16x32_bf16 v[56:59], v[182:185], v[128:131], v[56:59]
	s_waitcnt lgkmcnt(2)
	v_mfma_f32_16x16x32_bf16 v[52:55], v[186:189], v[128:131], v[52:55]
	ds_read_b128 v[140:143], v216 offset:48192
	s_waitcnt lgkmcnt(2)
	v_mfma_f32_16x16x32_bf16 v[48:51], v[174:177], v[132:135], v[48:51]
	v_mfma_f32_16x16x32_bf16 v[44:47], v[178:181], v[132:135], v[44:47]
	v_mfma_f32_16x16x32_bf16 v[40:43], v[182:185], v[132:135], v[40:43]
	v_mfma_f32_16x16x32_bf16 v[36:39], v[186:189], v[132:135], v[36:39]
	s_waitcnt lgkmcnt(1)
	v_mfma_f32_16x16x32_bf16 v[28:31], v[174:177], v[136:139], v[28:31]
	v_mfma_f32_16x16x32_bf16 v[24:27], v[178:181], v[136:139], v[24:27]
	v_mfma_f32_16x16x32_bf16 v[16:19], v[182:185], v[136:139], v[16:19]
	v_mfma_f32_16x16x32_bf16 v[12:15], v[186:189], v[136:139], v[12:15]
	s_waitcnt lgkmcnt(0)
	v_mfma_f32_16x16x32_bf16 v[8:11], v[174:177], v[140:143], v[8:11]
	v_mfma_f32_16x16x32_bf16 v[4:7], v[178:181], v[140:143], v[4:7]
	v_mfma_f32_16x16x32_bf16 v[32:35], v[182:185], v[140:143], v[32:35]
	v_mfma_f32_16x16x32_bf16 v[20:23], v[186:189], v[140:143], v[20:23]
	s_waitcnt vmcnt(0) lgkmcnt(0)
	s_barrier
	s_add_i32 s6, s6, 2
	s_cmp_lt_u32 s6, 14
	s_cbranch_scc1 .Lip_loop
; #define LAS __attribute__((address_space(3)))
; __device__ __forceinline__ s16x4 lds_tr(lds_cptr p) { return __builtin_bit_cast(s16x4, __builtin_amdgcn_ds_read_tr16_b64_v4i16((LAS s16x4*)p)); }
;     ...
;     auto compute = [&]() __attribute__((always_inline)) {
; #pragma unroll
;         for (int kh = 0; kh < 2; ++kh) {
;             bf16x8 af[4], bfr[4];
; #pragma unroll
;             for (int m = 0; m < 4; ++m) af[m] = *(const LAS bf16x8*)(la + kh * GA_KH + m * 1024);
; #pragma unroll
;             for (int n = 0; n < 4; ++n) {
;                 const s16x4 r0 = lds_tr(lb + kh * 32 * GB_ST + n * 32), r1 = lds_tr(lb + kh * 32 * GB_ST + n * 32 + bsw);
;                 bfr[n] = (bf16x8){r0[0], r0[1], r0[2], r0[3], r1[0], r1[1], r1[2], r1[3]};
;             }
; #pragma unroll
;             for (int m = 0; m < 4; ++m)
; #pragma unroll
;                 for (int n = 0; n < 4; ++n) acc[m][n] = __builtin_amdgcn_mfma_f32_16x16x32_bf16(bfr[n], af[m], acc[m][n], 0, 0, 0);
;         }
;     };
;     ...
;     if (DEEP == 1) {
;         gloadA(0, ra0); gloadB(0, rb0); gloadA(1, ra1);
;         for (int kt = 0; kt < nk; kt += 2) {
;             __syncthreads();
;             lstore(ra0, rb0);
;             __syncthreads();
;             gloadB(kt + 1, rb0);
;             if (kt + 2 < nk) gloadA(kt + 2, ra0);
;             compute();
	s_add_u32 m0, s98, 0x9000
	ds_read_b64_tr_b16 v[158:159], v214 offset:16512
	ds_read_b64_tr_b16 v[160:161], v214 offset:17536
	ds_read_b128 v[128:131], v216
	ds_read_b64_tr_b16 v[162:163], v215 offset:16512
	ds_read_b64_tr_b16 v[164:165], v215 offset:17536
	s_waitcnt lgkmcnt(2)
	v_mfma_f32_16x16x32_bf16 v[64:67], v[158:161], v[128:131], v[64:67]
	global_load_lds_dwordx4 v206, s[44:45]
	s_add_u32 m0, s98, 0xb040
	ds_read_b64_tr_b16 v[166:167], v217 offset:16512
	ds_read_b64_tr_b16 v[168:169], v217 offset:17536
	s_waitcnt lgkmcnt(2)
	v_mfma_f32_16x16x32_bf16 v[60:63], v[162:165], v[128:131], v[60:63]
	global_load_lds_dwordx4 v207, s[44:45]
	s_add_u32 m0, s98, 0x9400
	ds_read_b64_tr_b16 v[170:171], v218 offset:16512
	ds_read_b64_tr_b16 v[172:173], v218 offset:17536
	s_waitcnt lgkmcnt(2)
	v_mfma_f32_16x16x32_bf16 v[56:59], v[166:169], v[128:131], v[56:59]
	global_load_lds_dwordx4 v208, s[44:45]
	s_add_u32 m0, s98, 0xb440
	ds_read_b128 v[132:135], v216 offset:1024
	s_waitcnt lgkmcnt(1)
	v_mfma_f32_16x16x32_bf16 v[52:55], v[170:173], v[128:131], v[52:55]
	global_load_lds_dwordx4 v209, s[44:45]
	s_add_u32 m0, s99, 0xd080
	ds_read_b128 v[136:139], v216 offset:2048
	s_waitcnt lgkmcnt(1)
	v_mfma_f32_16x16x32_bf16 v[48:51], v[158:161], v[132:135], v[48:51]
	global_load_lds_dwordx4 v210, s[46:47]
	s_add_u32 m0, s99, 0xd480
	ds_read_b128 v[140:143], v216 offset:3072
	v_mfma_f32_16x16x32_bf16 v[44:47], v[162:165], v[132:135], v[44:47]
	global_load_lds_dwordx4 v211, s[46:47]
	s_add_u32 m0, s99, 0xd880
	ds_read_b64_tr_b16 v[174:175], v214 offset:24704
	ds_read_b64_tr_b16 v[176:177], v214 offset:25728
	v_mfma_f32_16x16x32_bf16 v[40:43], v[166:169], v[132:135], v[40:43]
	global_load_lds_dwordx4 v212, s[46:47]
	s_add_u32 m0, s99, 0xdc80
	ds_read_b64_tr_b16 v[178:179], v215 offset:24704
	ds_read_b64_tr_b16 v[180:181], v215 offset:25728
	v_mfma_f32_16x16x32_bf16 v[36:39], v[170:173], v[132:135], v[36:39]
	global_load_lds_dwordx4 v213, s[46:47]
	s_add_u32 s44, s44, 0x80
	s_addc_u32 s45, s45, 0
	s_add_u32 s46, s46, 0x48000
	s_addc_u32 s47, s47, 0
	ds_read_b128 v[128:131], v216 offset:8256
	s_waitcnt lgkmcnt(6)
	v_mfma_f32_16x16x32_bf16 v[28:31], v[158:161], v[136:139], v[28:31]
	ds_read_b64_tr_b16 v[182:183], v217 offset:24704
	ds_read_b64_tr_b16 v[184:185], v217 offset:25728
	v_mfma_f32_16x16x32_bf16 v[24:27], v[162:165], v[136:139], v[24:27]
	ds_read_b64_tr_b16 v[186:187], v218 offset:24704
	ds_read_b64_tr_b16 v[188:189], v218 offset:25728
	v_mfma_f32_16x16x32_bf16 v[16:19], v[166:169], v[136:139], v[16:19]
	v_mfma_f32_16x16x32_bf16 v[12:15], v[170:173], v[136:139], v[12:15]
	ds_read_b128 v[132:135], v216 offset:9280
	s_waitcnt lgkmcnt(10)
	v_mfma_f32_16x16x32_bf16 v[8:11], v[158:161], v[140:143], v[8:11]
	v_mfma_f32_16x16x32_bf16 v[4:7], v[162:165], v[140:143], v[4:7]
	v_mfma_f32_16x16x32_bf16 v[32:35], v[166:169], v[140:143], v[32:35]
	v_mfma_f32_16x16x32_bf16 v[20:23], v[170:173], v[140:143], v[20:23]
	ds_read_b128 v[136:139], v216 offset:10304
	s_waitcnt lgkmcnt(6)
	v_mfma_f32_16x16x32_bf16 v[64:67], v[174:177], v[128:131], v[64:67]
	v_mfma_f32_16x16x32_bf16 v[60:63], v[178:181], v[128:131], v[60:63]
	s_waitcnt lgkmcnt(4)
	v_mfma_f32_16x16x32_bf16 v[56:59], v[182:185], v[128:131], v[56:59]
	s_waitcnt lgkmcnt(2)
	v_mfma_f32_16x16x32_bf16 v[52:55], v[186:189], v[128:131], v[52:55]
	ds_read_b128 v[140:143], v216 offset:11328
	s_waitcnt lgkmcnt(2)
	v_mfma_f32_16x16x32_bf16 v[48:51], v[174:177], v[132:135], v[48:51]
	v_mfma_f32_16x16x32_bf16 v[44:47], v[178:181], v[132:135], v[44:47]
	v_mfma_f32_16x16x32_bf16 v[40:43], v[182:185], v[132:135], v[40:43]
	v_mfma_f32_16x16x32_bf16 v[36:39], v[186:189], v[132:135], v[36:39]
	s_waitcnt lgkmcnt(1)
	v_mfma_f32_16x16x32_bf16 v[28:31], v[174:177], v[136:139], v[28:31]
	v_mfma_f32_16x16x32_bf16 v[24:27], v[178:181], v[136:139], v[24:27]
	v_mfma_f32_16x16x32_bf16 v[16:19], v[182:185], v[136:139], v[16:19]
	v_mfma_f32_16x16x32_bf16 v[12:15], v[186:189], v[136:139], v[12:15]
	s_waitcnt lgkmcnt(0)
	v_mfma_f32_16x16x32_bf16 v[8:11], v[174:177], v[140:143], v[8:11]
	v_mfma_f32_16x16x32_bf16 v[4:7], v[178:181], v[140:143], v[4:7]
	v_mfma_f32_16x16x32_bf16 v[32:35], v[182:185], v[140:143], v[32:35]
	v_mfma_f32_16x16x32_bf16 v[20:23], v[186:189], v[140:143], v[20:23]
	s_waitcnt vmcnt(0) lgkmcnt(0)
	s_barrier
;     template <class T> __device__ __forceinline__ T* w(size_t off) const { return (T*)(p->ws + off); }
;     ...
;             __syncthreads();
;             lstore(ra1, rb0);
;             __syncthreads();
;             if (kt + 2 < nk) gloadB(kt + 2, rb0);
;             if (kt + 3 < nk) gloadA(kt + 3, ra1);
;             compute();
;         }
; __device__ __forceinline__ void ph_inproj_mfma(const Ctx& c, int layer, int tile, unsigned char* lds) {
;     const int mt = tile / 18, nt = tile % 18;
;     const bf16* HA = c.w<bf16>(WS_HA) + (size_t)mt * 128 * D;
;     f32x4 acc[4][4];
;     const int vc = nt * 128 + (c.tid & 15) * 8;
;     gemm_tile<false, 1>(c.tid, lds, HA, [&](int r) __attribute__((always_inline)) { return (unsigned)(r * D); }, c.w<bf16>(WS_BIN) + (size_t)layer * D * DINV, (unsigned)vc, DINV, true, D, acc);
	ds_read_b64_tr_b16 v[158:159], v214 offset:53376
	ds_read_b64_tr_b16 v[160:161], v214 offset:54400
	ds_read_b128 v[128:131], v216 offset:36864
	ds_read_b64_tr_b16 v[162:163], v215 offset:53376
	ds_read_b64_tr_b16 v[164:165], v215 offset:54400
	s_waitcnt lgkmcnt(2)
	v_mfma_f32_16x16x32_bf16 v[64:67], v[158:161], v[128:131], v[64:67]
	ds_read_b64_tr_b16 v[166:167], v217 offset:53376
	ds_read_b64_tr_b16 v[168:169], v217 offset:54400
	s_waitcnt lgkmcnt(2)
	v_mfma_f32_16x16x32_bf16 v[60:63], v[162:165], v[128:131], v[60:63]
	ds_read_b64_tr_b16 v[170:171], v218 offset:53376
	ds_read_b64_tr_b16 v[172:173], v218 offset:54400
	s_waitcnt lgkmcnt(2)
	v_mfma_f32_16x16x32_bf16 v[56:59], v[166:169], v[128:131], v[56:59]
	ds_read_b128 v[132:135], v216 offset:37888
	s_waitcnt lgkmcnt(1)
	v_mfma_f32_16x16x32_bf16 v[52:55], v[170:173], v[128:131], v[52:55]
	ds_read_b128 v[136:139], v216 offset:38912
	s_waitcnt lgkmcnt(1)
	v_mfma_f32_16x16x32_bf16 v[48:51], v[158:161], v[132:135], v[48:51]
	ds_read_b128 v[140:143], v216 offset:39936
	v_mfma_f32_16x16x32_bf16 v[44:47], v[162:165], v[132:135], v[44:47]
	ds_read_b64_tr_b16 v[174:175], v214 offset:61568
	ds_read_b64_tr_b16 v[176:177], v214 offset:62592
	v_mfma_f32_16x16x32_bf16 v[40:43], v[166:169], v[132:135], v[40:43]
	ds_read_b64_tr_b16 v[178:179], v215 offset:61568
	ds_read_b64_tr_b16 v[180:181], v215 offset:62592
	v_mfma_f32_16x16x32_bf16 v[36:39], v[170:173], v[132:135], v[36:39]
	ds_read_b128 v[128:131], v216 offset:45120
	s_waitcnt lgkmcnt(6)
	v_mfma_f32_16x16x32_bf16 v[28:31], v[158:161], v[136:139], v[28:31]
	ds_read_b64_tr_b16 v[182:183], v217 offset:61568
	ds_read_b64_tr_b16 v[184:185], v217 offset:62592
	v_mfma_f32_16x16x32_bf16 v[24:27], v[162:165], v[136:139], v[24:27]
	ds_read_b64_tr_b16 v[186:187], v218 offset:61568
	ds_read_b64_tr_b16 v[188:189], v218 offset:62592
	v_mfma_f32_16x16x32_bf16 v[16:19], v[166:169], v[136:139], v[16:19]
	v_mfma_f32_16x16x32_bf16 v[12:15], v[170:173], v[136:139], v[12:15]
	ds_read_b128 v[132:135], v216 offset:46144
	s_waitcnt lgkmcnt(10)
	v_mfma_f32_16x16x32_bf16 v[8:11], v[158:161], v[140:143], v[8:11]
	v_mfma_f32_16x16x32_bf16 v[4:7], v[162:165], v[140:143], v[4:7]
	v_mfma_f32_16x16x32_bf16 v[32:35], v[166:169], v[140:143], v[32:35]
	v_mfma_f32_16x16x32_bf16 v[20:23], v[170:173], v[140:143], v[20:23]
	ds_read_b128 v[136:139], v216 offset:47168
	s_waitcnt lgkmcnt(6)
	v_mfma_f32_16x16x32_bf16 v[64:67], v[174:177], v[128:131], v[64:67]
	v_mfma_f32_16x16x32_bf16 v[60:63], v[178:181], v[128:131], v[60:63]
	s_waitcnt lgkmcnt(4)
	v_mfma_f32_16x16x32_bf16 v[56:59], v[182:185], v[128:131], v[56:59]
	s_waitcnt lgkmcnt(2)
	v_mfma_f32_16x16x32_bf16 v[52:55], v[186:189], v[128:131], v[52:55]
	ds_read_b128 v[140:143], v216 offset:48192
	s_waitcnt lgkmcnt(2)
	v_mfma_f32_16x16x32_bf16 v[48:51], v[174:177], v[132:135], v[48:51]
	v_mfma_f32_16x16x32_bf16 v[44:47], v[178:181], v[132:135], v[44:47]
	v_mfma_f32_16x16x32_bf16 v[40:43], v[182:185], v[132:135], v[40:43]
	v_mfma_f32_16x16x32_bf16 v[36:39], v[186:189], v[132:135], v[36:39]
	s_waitcnt lgkmcnt(1)
	v_mfma_f32_16x16x32_bf16 v[28:31], v[174:177], v[136:139], v[28:31]
	v_mfma_f32_16x16x32_bf16 v[24:27], v[178:181], v[136:139], v[24:27]
	v_mfma_f32_16x16x32_bf16 v[16:19], v[182:185], v[136:139], v[16:19]
	v_mfma_f32_16x16x32_bf16 v[12:15], v[186:189], v[136:139], v[12:15]
	s_waitcnt lgkmcnt(0)
	v_mfma_f32_16x16x32_bf16 v[8:11], v[174:177], v[140:143], v[8:11]
	v_mfma_f32_16x16x32_bf16 v[4:7], v[178:181], v[140:143], v[4:7]
	v_mfma_f32_16x16x32_bf16 v[32:35], v[182:185], v[140:143], v[32:35]
	v_mfma_f32_16x16x32_bf16 v[20:23], v[186:189], v[140:143], v[20:23]
	s_waitcnt vmcnt(0) lgkmcnt(0)
	s_barrier
	s_add_i32 s6, s60, s3
	s_cmpk_gt_i32 s6, 0x98f
	s_cbranch_scc1 .Lip_nopf
	s_mul_hi_i32 s100, s6, 0x38e38e39
	s_lshr_b32 s101, s100, 31
	s_ashr_i32 s100, s100, 2
	s_add_i32 s100, s100, s101
	s_mul_i32 s101, s100, 18
	s_sub_i32 s6, s6, s101
	s_lshl_b32 s6, s6, 8
	s_ashr_i32 s101, s100, 31
	s_lshl_b64 s[100:101], s[100:101], 18
	s_add_u32 s100, s42, s100
	s_addc_u32 s101, s43, s101
	s_add_u32 s100, s100, 0x45c6000
	s_addc_u32 s101, s101, 0
	s_add_u32 m0, s98, 0x0
	s_nop 0
	global_load_lds_dwordx4 v206, s[100:101]
	s_add_u32 m0, s98, 0x2040
	s_nop 0
	global_load_lds_dwordx4 v207, s[100:101]
	s_add_u32 m0, s98, 0x400
	s_nop 0
	global_load_lds_dwordx4 v208, s[100:101]
	s_add_u32 m0, s98, 0x2440
	s_nop 0
	global_load_lds_dwordx4 v209, s[100:101]
	s_add_u32 s100, s42, s59
	s_addc_u32 s101, s43, s58
	s_add_u32 s100, s100, 0x18095100
	s_addc_u32 s101, s101, 0
	s_add_u32 s100, s100, s6
	s_addc_u32 s101, s101, 0
	s_add_u32 m0, s99, 0x4080
	s_nop 0
	global_load_lds_dwordx4 v210, s[100:101]
	s_add_u32 m0, s99, 0x4480
	s_nop 0
	global_load_lds_dwordx4 v211, s[100:101]
	s_add_u32 m0, s99, 0x4880
	s_nop 0
	global_load_lds_dwordx4 v212, s[100:101]
	s_add_u32 m0, s99, 0x4c80
	s_nop 0
	global_load_lds_dwordx4 v213, s[100:101]
	s_mov_b32 s101, 1
	s_branch .Lip_pfdone
; __device__ __forceinline__ uint2 pack4(const f32x4 v) { uint2 o; o.x = pk2bf(v[0], v[1]); o.y = pk2bf(v[2], v[3]); return o; }
;     template <class T> __device__ __forceinline__ T* w(size_t off) const { return (T*)(p->ws + off); }
; __device__ __forceinline__ void ph_inproj_mfma(const Ctx& c, int layer, int tile, unsigned char* lds) {
;     ...
;     const int lane = c.tid & 63, wid = c.tid >> 6, wr = wid >> 1, wc = wid & 1, fr = lane & 15, fq = lane >> 4;
;     const int n0 = mt * 128, b = n0 / LT, pos0 = n0 % LT;
;     if (nt < 2) {
;     ...
;         bf16* dst; int ld, col0;
;         if (nt < 8) { dst = c.w<bf16>(WS_Z); ld = 256; col0 = (nt - 6) * 128; } else { dst = c.w<bf16>(WS_XBR); ld = 768; col0 = (nt - 8) * 128; }
; #pragma unroll
;         for (int m = 0; m < 4; ++m) { const size_t row = (size_t)n0 + wr * 64 + m * 16 + fr;
; #pragma unroll
;             for (int n = 0; n < 4; ++n) *(uint2*)(dst + row * ld + col0 + wc * 64 + n * 16 + fq * 4) = pack4(acc[m][n]); }
.Lip_nopf:
	s_mov_b32 s101, 0
.Lip_pfdone:
.LBB0_553:
	s_mul_hi_i32 s1, s60, 0xd62b80d7
	s_add_i32 s1, s1, s60
	s_lshl_b32 s0, s28, 7
	s_lshr_b32 s6, s1, 31
	s_ashr_i32 s1, s1, 9
	s_add_i32 s28, s1, s6
	s_mul_hi_i32 s1, s0, 0x78787879
	s_lshr_b32 s6, s1, 31
	s_ashr_i32 s1, s1, 11
	s_add_i32 s1, s1, s6
	s_mulk_i32 s1, 0x1100
	s_sub_i32 s16, s0, s1
	v_ashrrev_i32_e32 v159, 7, v147
	v_bfe_u32 v158, v147, 6, 1
	s_cmp_gt_i32 s17, 1
	s_mov_b64 s[6:7], -1
	s_cbranch_scc0 .LBB0_587
	v_sub_co_u32_e64 v2, s[44:45], s17, 14
	v_cmp_lt_u32_e32 vcc, -9, v2
	s_cbranch_vccz .LBB0_556
	s_cmp_lt_u32 s17, 8
	s_cselect_b64 s[6:7], -1, 0
	s_and_b64 s[6:7], s[6:7], exec
	s_mov_b32 s1, 0x67c6000
	s_cselect_b32 s1, s1, 0x7046000
	s_movk_i32 s6, 0xfd00
	s_movk_i32 s7, 0x300
	s_cselect_b32 s6, s6, 0xfffffc00
	s_cselect_b32 s7, 0x100, s7
	s_add_u32 s18, s42, s1
	v_lshlrev_b32_e32 v68, 6, v159
	s_addc_u32 s19, s43, 0
	s_add_i32 s72, s6, s61
	s_ashr_i32 s1, s0, 31
	v_ashrrev_i32_e32 v69, 31, v68
	v_lshl_add_u64 v[68:69], v[68:69], 0, s[0:1]
	s_lshl_b64 s[0:1], s[72:73], 1
	s_add_u32 s0, s18, s0
	v_or_b32_e32 v68, v68, v155
	s_addc_u32 s1, s19, s1
	v_lshlrev_b32_e32 v2, 7, v158
	v_lshl_add_u64 v[70:71], s[0:1], 0, v[2:3]
	v_mov_b32_e32 v119, v3
	v_mad_u64_u32 v[72:73], s[0:1], v68, s7, 0
	v_lshl_add_u64 v[70:71], v[70:71], 0, v[118:119]
	v_mad_i32_i24 v73, v69, s7, v73
	v_lshl_add_u64 v[68:69], v[72:73], 1, v[70:71]
	v_cvt_pk_bf16_f32 v70, v64, v65
	v_cvt_pk_bf16_f32 v71, v66, v67
	global_store_dwordx2 v[68:69], v[70:71], off
	v_cvt_pk_bf16_f32 v70, v60, v61
	v_cvt_pk_bf16_f32 v71, v62, v63
	global_store_dwordx2 v[68:69], v[70:71], off offset:32
	v_cvt_pk_bf16_f32 v70, v56, v57
	v_cvt_pk_bf16_f32 v71, v58, v59
	global_store_dwordx2 v[68:69], v[70:71], off offset:64
	v_cvt_pk_bf16_f32 v70, v52, v53
	v_cvt_pk_bf16_f32 v71, v54, v55
	s_lshl_b32 s72, s7, 5
	global_store_dwordx2 v[68:69], v[70:71], off offset:96
	v_lshl_add_u64 v[68:69], v[68:69], 0, s[72:73]
	v_cvt_pk_bf16_f32 v70, v48, v49
	v_cvt_pk_bf16_f32 v71, v50, v51
	global_store_dwordx2 v[68:69], v[70:71], off
	v_cvt_pk_bf16_f32 v70, v44, v45
	v_cvt_pk_bf16_f32 v71, v46, v47
	global_store_dwordx2 v[68:69], v[70:71], off offset:32
	v_cvt_pk_bf16_f32 v70, v40, v41
	v_cvt_pk_bf16_f32 v71, v42, v43
	global_store_dwordx2 v[68:69], v[70:71], off offset:64
	v_cvt_pk_bf16_f32 v70, v36, v37
	v_cvt_pk_bf16_f32 v71, v38, v39
	global_store_dwordx2 v[68:69], v[70:71], off offset:96
	v_lshl_add_u64 v[68:69], v[68:69], 0, s[72:73]
	v_cvt_pk_bf16_f32 v70, v28, v29
	v_cvt_pk_bf16_f32 v71, v30, v31
	global_store_dwordx2 v[68:69], v[70:71], off
	v_cvt_pk_bf16_f32 v70, v24, v25
	v_cvt_pk_bf16_f32 v71, v26, v27
	global_store_dwordx2 v[68:69], v[70:71], off offset:32
	v_cvt_pk_bf16_f32 v70, v16, v17
	v_cvt_pk_bf16_f32 v71, v18, v19
	global_store_dwordx2 v[68:69], v[70:71], off offset:64
	v_cvt_pk_bf16_f32 v70, v12, v13
	v_cvt_pk_bf16_f32 v71, v14, v15
	global_store_dwordx2 v[68:69], v[70:71], off offset:96
	v_lshl_add_u64 v[68:69], v[68:69], 0, s[72:73]
	v_cvt_pk_bf16_f32 v70, v8, v9
	v_cvt_pk_bf16_f32 v71, v10, v11
	global_store_dwordx2 v[68:69], v[70:71], off
	v_cvt_pk_bf16_f32 v70, v4, v5
	v_cvt_pk_bf16_f32 v71, v6, v7
	global_store_dwordx2 v[68:69], v[70:71], off offset:32
	v_cvt_pk_bf16_f32 v70, v32, v33
	v_cvt_pk_bf16_f32 v71, v34, v35
	global_store_dwordx2 v[68:69], v[70:71], off offset:64
	v_cvt_pk_bf16_f32 v70, v20, v21
	v_cvt_pk_bf16_f32 v71, v22, v23
	global_store_dwordx2 v[68:69], v[70:71], off offset:96
	s_mov_b64 s[6:7], 0
